# prep without the code/kernarg touch loads (to see whether they matter); otherwise v35
# baseline (speedup 1.0000x reference)
.Lprep_ld_done:
	s_waitcnt vmcnt(0)
	v_pk_mul_f32 v[12:13], v[12:13], v[16:17] op_sel_hi:[1,0]
	v_pk_mul_f32 v[14:15], v[14:15], v[16:17] op_sel_hi:[1,0]
	v_pk_fma_f32 v[8:9], v[8:9], v[6:7], v[12:13] op_sel_hi:[1,0,1]
	v_pk_fma_f32 v[10:11], v[10:11], v[6:7], v[14:15] op_sel_hi:[1,0,1]
	s_nop 1
	v_add_f32_dpp v8, v8, v8 row_ror:8 row_mask:0xf bank_mask:0xf bound_ctrl:1
	v_add_f32_dpp v9, v9, v9 row_ror:8 row_mask:0xf bank_mask:0xf bound_ctrl:1
	v_add_f32_dpp v10, v10, v10 row_ror:8 row_mask:0xf bank_mask:0xf bound_ctrl:1
	v_add_f32_dpp v11, v11, v11 row_ror:8 row_mask:0xf bank_mask:0xf bound_ctrl:1
	v_mov_b32_e32 v12, v8
	v_mov_b32_e32 v13, v9
	v_mov_b32_e32 v14, v10
	v_mov_b32_e32 v15, v11
	v_permlane16_swap_b32_e32 v8, v12
	v_permlane16_swap_b32_e32 v9, v13
	v_permlane16_swap_b32_e32 v10, v14
	v_permlane16_swap_b32_e32 v11, v15
	v_add_f32_e32 v8, v8, v12
	v_add_f32_e32 v9, v9, v13
	v_add_f32_e32 v10, v10, v14
	v_add_f32_e32 v11, v11, v15
	v_mov_b32_e32 v12, v8
	v_mov_b32_e32 v13, v9
	v_mov_b32_e32 v14, v10
	v_mov_b32_e32 v15, v11
	v_permlane32_swap_b32_e32 v8, v12
	v_permlane32_swap_b32_e32 v9, v13
	v_permlane32_swap_b32_e32 v10, v14
	v_permlane32_swap_b32_e32 v11, v15
	v_add_f32_e32 v8, v8, v12
	v_add_f32_e32 v9, v9, v13
	v_add_f32_e32 v10, v10, v14
	v_add_f32_e32 v11, v11, v15
	v_lshlrev_b32_e32 v21, 4, v19
	v_lshl_add_u32 v21, v20, 7, v21
	v_cmp_gt_u32_e32 vcc, 8, v19
	s_and_saveexec_b64 s[20:21], vcc
	ds_write_b128 v21, v[8:11]
	s_mov_b64 exec, s[20:21]
	s_cmp_lg_u32 s2, 0
	s_cbranch_scc1 .Lprep_bar
	v_mul_f32_e32 v23, v23, v24
	s_nop 1
	v_add_f32_dpp v23, v23, v23 quad_perm:[1,0,3,2] row_mask:0xf bank_mask:0xf bound_ctrl:1
	s_nop 1
	v_add_f32_dpp v23, v23, v23 quad_perm:[2,3,0,1] row_mask:0xf bank_mask:0xf bound_ctrl:1
	s_nop 1
	v_add_f32_dpp v23, v23, v23 row_ror:4 row_mask:0xf bank_mask:0xf bound_ctrl:1
	s_nop 1
	v_add_f32_dpp v23, v23, v23 row_ror:8 row_mask:0xf bank_mask:0xf bound_ctrl:1
	v_mov_b32_e32 v24, v23
	s_nop 1
	v_permlane16_swap_b32_e32 v23, v24
	v_add_f32_e32 v23, v23, v24
	v_mov_b32_e32 v24, v23
	s_nop 1
	v_permlane32_swap_b32_e32 v23, v24
	v_add_f32_e32 v23, v23, v24
	v_lshlrev_b32_e32 v22, 2, v20
	v_cmp_eq_u32_e32 vcc, 0, v19
	s_and_saveexec_b64 s[20:21], vcc
	ds_write_b32 v22, v23 offset:2048
	s_mov_b64 exec, s[20:21]

.Lprep_done:
.Lprep_exit:
	s_endpgm
